# grid barrier: non-leader workgroups poll the top-level generation word directly instead of the per-XCD word (one release hop less)
# speedup vs baseline: 1.0555x; 1.0010x over previous
.LBB0_48:
	s_lshl_b32 s4, s22, 8
	s_add_u32 s4, s2, s4
	s_addc_u32 s5, s3, 0
	v_mov_b32_e32 v2, 0x1000
	v_mov_b32_e32 v4, 1
	global_atomic_add v4, v2, v4, s[4:5] offset:1024 sc0
	v_cvt_f32_u32_e32 v2, v3
	v_sub_u32_e32 v5, 0, v3
	v_rcp_iflag_f32_e32 v2, v2
	s_nop 0
	v_mul_f32_e32 v2, 0x4f7ffffe, v2
	v_cvt_u32_f32_e32 v2, v2
	v_mul_lo_u32 v5, v5, v2
	v_mul_hi_u32 v5, v2, v5
	v_add_u32_e32 v2, v2, v5
	s_waitcnt vmcnt(0)
	v_mul_hi_u32 v2, v4, v2
	v_mul_lo_u32 v5, v2, v3
	v_sub_u32_e32 v5, v4, v5
	v_add_u32_e32 v6, 1, v2
	v_cmp_ge_u32_e32 vcc, v5, v3
	v_add_u32_e32 v4, 1, v4
	s_nop 0
	v_cndmask_b32_e32 v2, v2, v6, vcc
	v_sub_u32_e32 v6, v5, v3
	v_cndmask_b32_e32 v5, v5, v6, vcc
	v_add_u32_e32 v6, 1, v2
	v_cmp_ge_u32_e32 vcc, v5, v3
	s_nop 1
	v_cndmask_b32_e32 v2, v2, v6, vcc
	v_mul_lo_u32 v5, v3, v2
	v_add_u32_e32 v3, v5, v3
	v_cmp_ne_u32_e32 vcc, v4, v3
	s_and_saveexec_b64 s[6:7], vcc
	s_xor_b64 s[6:7], exec, s[6:7]
	s_cbranch_execz .LBB0_62
	s_waitcnt lgkmcnt(0)
	v_mov_b32_e32 v1, 0x3100
	global_load_dword v1, v1, s[2:3] offset:1024 sc1
	s_add_u32 s10, s2, 0x3500
	s_addc_u32 s11, s3, 0
	s_waitcnt vmcnt(0)
	v_cmp_eq_u32_e32 vcc, v1, v2
	s_and_saveexec_b64 s[8:9], vcc
	s_cbranch_execz .LBB0_61
	s_mov_b32 s23, 1
	s_mov_b64 s[12:13], 0
	v_mov_b32_e32 v1, 0
	s_branch .LBB0_52

.LBB0_200:
	v_readlane_b32 s0, v253, 49
	s_lshl_b32 s0, s0, 2
	s_add_u32 s6, s4, s0
	s_addc_u32 s7, s5, 0
	v_mov_b32_e32 v1, 0x1000
	global_atomic_add v4, v1, v250, s[6:7] offset:1024 sc0
	v_cvt_f32_u32_e32 v1, v3
	v_sub_u32_e32 v5, 0, v3
	v_rcp_iflag_f32_e32 v1, v1
	s_nop 0
	v_mul_f32_e32 v1, 0x4f7ffffe, v1
	v_cvt_u32_f32_e32 v1, v1
	v_mul_lo_u32 v5, v5, v1
	v_mul_hi_u32 v5, v1, v5
	v_add_u32_e32 v1, v1, v5
	s_waitcnt vmcnt(0)
	v_mul_hi_u32 v1, v4, v1
	v_mul_lo_u32 v5, v1, v3
	v_sub_u32_e32 v5, v4, v5
	v_add_u32_e32 v6, 1, v1
	v_cmp_ge_u32_e32 vcc, v5, v3
	v_add_u32_e32 v4, 1, v4
	s_nop 0
	v_cndmask_b32_e32 v1, v1, v6, vcc
	v_sub_u32_e32 v6, v5, v3
	v_cndmask_b32_e32 v5, v5, v6, vcc
	v_add_u32_e32 v6, 1, v1
	v_cmp_ge_u32_e32 vcc, v5, v3
	s_nop 1
	v_cndmask_b32_e32 v1, v1, v6, vcc
	v_mul_lo_u32 v5, v3, v1
	v_add_u32_e32 v3, v5, v3
	v_cmp_ne_u32_e32 vcc, v4, v3
	s_and_saveexec_b64 s[0:1], vcc
	s_xor_b64 s[8:9], exec, s[0:1]
	s_cbranch_execz .LBB0_214
	s_waitcnt lgkmcnt(0)
	v_mov_b32_e32 v2, 0x3100
	global_load_dword v2, v2, s[4:5] offset:1024 sc1
	s_add_u32 s14, s4, 0x3500
	s_addc_u32 s15, s5, 0
	s_waitcnt vmcnt(0)
	v_cmp_eq_u32_e32 vcc, v2, v1
	s_and_saveexec_b64 s[10:11], vcc
	s_cbranch_execz .LBB0_213
	s_mov_b32 s29, 1
	s_mov_b64 s[18:19], 0
	s_branch .LBB0_204

.LBB0_894:
	v_readlane_b32 s0, v253, 49
	s_lshl_b32 s0, s0, 2
	s_add_u32 s8, s4, s0
	s_addc_u32 s9, s5, 0
	v_mov_b32_e32 v1, 0x1000
	global_atomic_add v4, v1, v250, s[8:9] offset:1024 sc0
	v_cvt_f32_u32_e32 v1, v3
	v_sub_u32_e32 v5, 0, v3
	v_rcp_iflag_f32_e32 v1, v1
	s_nop 0
	v_mul_f32_e32 v1, 0x4f7ffffe, v1
	v_cvt_u32_f32_e32 v1, v1
	v_mul_lo_u32 v5, v5, v1
	v_mul_hi_u32 v5, v1, v5
	v_add_u32_e32 v1, v1, v5
	s_waitcnt vmcnt(0)
	v_mul_hi_u32 v1, v4, v1
	v_mul_lo_u32 v5, v1, v3
	v_sub_u32_e32 v5, v4, v5
	v_add_u32_e32 v6, 1, v1
	v_cmp_ge_u32_e32 vcc, v5, v3
	v_add_u32_e32 v4, 1, v4
	s_nop 0
	v_cndmask_b32_e32 v1, v1, v6, vcc
	v_sub_u32_e32 v6, v5, v3
	v_cndmask_b32_e32 v5, v5, v6, vcc
	v_add_u32_e32 v6, 1, v1
	v_cmp_ge_u32_e32 vcc, v5, v3
	s_nop 1
	v_cndmask_b32_e32 v1, v1, v6, vcc
	v_mul_lo_u32 v5, v3, v1
	v_add_u32_e32 v3, v5, v3
	v_cmp_ne_u32_e32 vcc, v4, v3
	s_and_saveexec_b64 s[0:1], vcc
	s_xor_b64 s[10:11], exec, s[0:1]
	s_cbranch_execz .LBB0_908
	s_waitcnt lgkmcnt(0)
	v_mov_b32_e32 v2, 0x3100
	global_load_dword v2, v2, s[4:5] offset:1024 sc1
	s_add_u32 s18, s4, 0x3500
	s_addc_u32 s19, s5, 0
	s_waitcnt vmcnt(0)
	v_cmp_eq_u32_e32 vcc, v2, v1
	s_and_saveexec_b64 s[14:15], vcc
	s_cbranch_execz .LBB0_907
	s_mov_b32 s31, 1
	s_mov_b64 s[22:23], 0
	s_branch .LBB0_898

.LBB0_1191:
	v_readlane_b32 s0, v253, 49
	s_lshl_b32 s0, s0, 2
	s_add_u32 s8, s4, s0
	s_addc_u32 s9, s5, 0
	v_mov_b32_e32 v1, 0x1000
	global_atomic_add v4, v1, v250, s[8:9] offset:1024 sc0
	v_cvt_f32_u32_e32 v1, v3
	v_sub_u32_e32 v5, 0, v3
	v_rcp_iflag_f32_e32 v1, v1
	s_nop 0
	v_mul_f32_e32 v1, 0x4f7ffffe, v1
	v_cvt_u32_f32_e32 v1, v1
	v_mul_lo_u32 v5, v5, v1
	v_mul_hi_u32 v5, v1, v5
	v_add_u32_e32 v1, v1, v5
	s_waitcnt vmcnt(0)
	v_mul_hi_u32 v1, v4, v1
	v_mul_lo_u32 v5, v1, v3
	v_sub_u32_e32 v5, v4, v5
	v_add_u32_e32 v6, 1, v1
	v_cmp_ge_u32_e32 vcc, v5, v3
	v_add_u32_e32 v4, 1, v4
	s_nop 0
	v_cndmask_b32_e32 v1, v1, v6, vcc
	v_sub_u32_e32 v6, v5, v3
	v_cndmask_b32_e32 v5, v5, v6, vcc
	v_add_u32_e32 v6, 1, v1
	v_cmp_ge_u32_e32 vcc, v5, v3
	s_nop 1
	v_cndmask_b32_e32 v1, v1, v6, vcc
	v_mul_lo_u32 v5, v3, v1
	v_add_u32_e32 v3, v5, v3
	v_cmp_ne_u32_e32 vcc, v4, v3
	s_and_saveexec_b64 s[0:1], vcc
	s_xor_b64 s[10:11], exec, s[0:1]
	s_cbranch_execz .LBB0_1205
	s_waitcnt lgkmcnt(0)
	v_mov_b32_e32 v2, 0x3100
	global_load_dword v2, v2, s[4:5] offset:1024 sc1
	s_add_u32 s18, s4, 0x3500
	s_addc_u32 s19, s5, 0
	s_waitcnt vmcnt(0)
	v_cmp_eq_u32_e32 vcc, v2, v1
	s_and_saveexec_b64 s[14:15], vcc
	s_cbranch_execz .LBB0_1204
	s_mov_b32 s30, 1
	s_mov_b64 s[22:23], 0
	s_branch .LBB0_1195

.LBB0_1756:
	v_readlane_b32 s0, v253, 49
	s_lshl_b32 s0, s0, 2
	s_add_u32 s6, s4, s0
	s_addc_u32 s7, s5, 0
	v_mov_b32_e32 v1, 0x1000
	global_atomic_add v4, v1, v250, s[6:7] offset:1024 sc0
	v_cvt_f32_u32_e32 v1, v3
	v_sub_u32_e32 v5, 0, v3
	v_rcp_iflag_f32_e32 v1, v1
	s_nop 0
	v_mul_f32_e32 v1, 0x4f7ffffe, v1
	v_cvt_u32_f32_e32 v1, v1
	v_mul_lo_u32 v5, v5, v1
	v_mul_hi_u32 v5, v1, v5
	v_add_u32_e32 v1, v1, v5
	s_waitcnt vmcnt(0)
	v_mul_hi_u32 v1, v4, v1
	v_mul_lo_u32 v5, v1, v3
	v_sub_u32_e32 v5, v4, v5
	v_add_u32_e32 v6, 1, v1
	v_cmp_ge_u32_e32 vcc, v5, v3
	v_add_u32_e32 v4, 1, v4
	s_nop 0
	v_cndmask_b32_e32 v1, v1, v6, vcc
	v_sub_u32_e32 v6, v5, v3
	v_cndmask_b32_e32 v5, v5, v6, vcc
	v_add_u32_e32 v6, 1, v1
	v_cmp_ge_u32_e32 vcc, v5, v3
	s_nop 1
	v_cndmask_b32_e32 v1, v1, v6, vcc
	v_mul_lo_u32 v5, v3, v1
	v_add_u32_e32 v3, v5, v3
	v_cmp_ne_u32_e32 vcc, v4, v3
	s_and_saveexec_b64 s[0:1], vcc
	s_xor_b64 s[8:9], exec, s[0:1]
	s_cbranch_execz .LBB0_1770
	s_waitcnt lgkmcnt(0)
	v_mov_b32_e32 v2, 0x3100
	global_load_dword v2, v2, s[4:5] offset:1024 sc1
	s_add_u32 s14, s4, 0x3500
	s_addc_u32 s15, s5, 0
	s_waitcnt vmcnt(0)
	v_cmp_eq_u32_e32 vcc, v2, v1
	s_and_saveexec_b64 s[10:11], vcc
	s_cbranch_execz .LBB0_1769
	s_mov_b32 s26, 1
	s_mov_b64 s[16:17], 0
	s_branch .LBB0_1760
